# baseline (speedup 1.0000x reference)
_Z13logits_kernelPKDv8_DF16bS1_PKfS3_PDv2_fS5_Pf:
	s_load_dwordx4 s[4:7], s[0:1], 0x0
	s_load_dwordx4 s[12:15], s[0:1], 0x10
	s_load_dwordx4 s[24:27], s[0:1], 0x20
	s_load_dwordx2 s[28:29], s[0:1], 0x30
	s_lshl_b32 s3, s2, 1
	s_and_b32 s3, s3, 14
	s_ashr_i32 s8, s2, 7
	s_bfe_u32 s10, s2, 0x40003
	s_add_i32 s3, s3, s8
	v_lshrrev_b32_e32 v1, 6, v0
	v_and_b32_e32 v2, 63, v0
	s_movk_i32 s11, 0x3000
	v_lshlrev_b32_e32 v2, 4, v2
	v_and_b32_e32 v5, 31, v0
	v_mad_u32_u24 v2, v1, s11, v2
	v_lshlrev_b32_e32 v5, 2, v5
	s_lshl_b32 s9, s3, 9
	v_add_u32_e32 v3, 0x1000, v2
	v_add_u32_e32 v4, 0x2000, v2
	v_add_u32_e32 v5, s9, v5
	s_mul_i32 s8, s10, 0xc000
	s_mul_i32 s9, s3, 0x30000
	s_waitcnt lgkmcnt(0)
	s_load_dword s22, s[14:15], 0x0
	global_load_dword v248, v5, s[12:13]
	global_load_dword v249, v5, s[12:13] offset:128
	global_load_dword v250, v5, s[12:13] offset:256
	global_load_dword v251, v5, s[12:13] offset:384
	s_add_u32 s4, s4, s8
	s_addc_u32 s5, s5, 0
	s_add_u32 s6, s6, s9
	s_addc_u32 s7, s7, 0
	s_add_u32 s16, s6, 0xc000
	s_addc_u32 s17, s7, 0
	s_add_u32 s18, s6, 0x18000
	s_addc_u32 s19, s7, 0
	s_add_u32 s20, s6, 0x24000
	s_addc_u32 s21, s7, 0
	global_load_dwordx4 v[8:11], v2, s[4:5]
	global_load_dwordx4 v[12:15], v2, s[4:5] offset:1024
	global_load_dwordx4 v[16:19], v2, s[4:5] offset:2048
	global_load_dwordx4 v[20:23], v2, s[4:5] offset:3072
	global_load_dwordx4 v[24:27], v3, s[4:5]
	global_load_dwordx4 v[28:31], v3, s[4:5] offset:1024
	global_load_dwordx4 v[32:35], v3, s[4:5] offset:2048
	global_load_dwordx4 v[36:39], v3, s[4:5] offset:3072
	global_load_dwordx4 v[40:43], v4, s[4:5]
	global_load_dwordx4 v[44:47], v4, s[4:5] offset:1024
	global_load_dwordx4 v[48:51], v4, s[4:5] offset:2048
	global_load_dwordx4 v[52:55], v4, s[4:5] offset:3072
	global_load_dwordx4 v[56:59], v2, s[6:7]
	global_load_dwordx4 v[104:107], v2, s[16:17]
	global_load_dwordx4 v[152:155], v2, s[18:19]
	global_load_dwordx4 v[200:203], v2, s[20:21]
	global_load_dwordx4 v[60:63], v2, s[6:7] offset:1024
	global_load_dwordx4 v[108:111], v2, s[16:17] offset:1024
	global_load_dwordx4 v[156:159], v2, s[18:19] offset:1024
	global_load_dwordx4 v[204:207], v2, s[20:21] offset:1024
	global_load_dwordx4 v[64:67], v2, s[6:7] offset:2048
	global_load_dwordx4 v[112:115], v2, s[16:17] offset:2048
	global_load_dwordx4 v[160:163], v2, s[18:19] offset:2048
	global_load_dwordx4 v[208:211], v2, s[20:21] offset:2048
	global_load_dwordx4 v[68:71], v2, s[6:7] offset:3072
	global_load_dwordx4 v[116:119], v2, s[16:17] offset:3072
	global_load_dwordx4 v[164:167], v2, s[18:19] offset:3072
	global_load_dwordx4 v[212:215], v2, s[20:21] offset:3072
	global_load_dwordx4 v[72:75], v3, s[6:7]
	global_load_dwordx4 v[120:123], v3, s[16:17]
	global_load_dwordx4 v[168:171], v3, s[18:19]
	global_load_dwordx4 v[216:219], v3, s[20:21]
	global_load_dwordx4 v[76:79], v3, s[6:7] offset:1024
	global_load_dwordx4 v[124:127], v3, s[16:17] offset:1024
	global_load_dwordx4 v[172:175], v3, s[18:19] offset:1024
	global_load_dwordx4 v[220:223], v3, s[20:21] offset:1024
	global_load_dwordx4 v[80:83], v3, s[6:7] offset:2048
	global_load_dwordx4 v[128:131], v3, s[16:17] offset:2048
	global_load_dwordx4 v[176:179], v3, s[18:19] offset:2048
	global_load_dwordx4 v[224:227], v3, s[20:21] offset:2048
	global_load_dwordx4 v[84:87], v3, s[6:7] offset:3072
	global_load_dwordx4 v[132:135], v3, s[16:17] offset:3072
	global_load_dwordx4 v[180:183], v3, s[18:19] offset:3072
	global_load_dwordx4 v[228:231], v3, s[20:21] offset:3072
	global_load_dwordx4 v[88:91], v4, s[6:7]
	global_load_dwordx4 v[136:139], v4, s[16:17]
	global_load_dwordx4 v[184:187], v4, s[18:19]
	global_load_dwordx4 v[232:235], v4, s[20:21]
	global_load_dwordx4 v[92:95], v4, s[6:7] offset:1024
	global_load_dwordx4 v[140:143], v4, s[16:17] offset:1024
	global_load_dwordx4 v[188:191], v4, s[18:19] offset:1024
	global_load_dwordx4 v[236:239], v4, s[20:21] offset:1024
	global_load_dwordx4 v[96:99], v4, s[6:7] offset:2048
	global_load_dwordx4 v[144:147], v4, s[16:17] offset:2048
	global_load_dwordx4 v[192:195], v4, s[18:19] offset:2048
	global_load_dwordx4 v[240:243], v4, s[20:21] offset:2048
	global_load_dwordx4 v[100:103], v4, s[6:7] offset:3072
	global_load_dwordx4 v[148:151], v4, s[16:17] offset:3072
	global_load_dwordx4 v[196:199], v4, s[18:19] offset:3072
	global_load_dwordx4 v[244:247], v4, s[20:21] offset:3072
	s_waitcnt vmcnt(47)
	v_mfma_f32_32x32x16_bf16 a[0:15], v[8:11], v[56:59], 0
	s_waitcnt vmcnt(46)
	v_mfma_f32_32x32x16_bf16 a[0:15], v[8:11], v[104:107], a[0:15]
	s_waitcnt vmcnt(45)
	v_mfma_f32_32x32x16_bf16 a[0:15], v[8:11], v[152:155], a[0:15]
	s_waitcnt vmcnt(44)
	v_mfma_f32_32x32x16_bf16 a[0:15], v[8:11], v[200:203], a[0:15]
	s_waitcnt vmcnt(43)
	v_mfma_f32_32x32x16_bf16 a[0:15], v[12:15], v[60:63], a[0:15]
	s_waitcnt vmcnt(42)
	v_mfma_f32_32x32x16_bf16 a[0:15], v[12:15], v[108:111], a[0:15]
	s_waitcnt vmcnt(41)
	v_mfma_f32_32x32x16_bf16 a[0:15], v[12:15], v[156:159], a[0:15]
	s_waitcnt vmcnt(40)
	v_mfma_f32_32x32x16_bf16 a[0:15], v[12:15], v[204:207], a[0:15]
	s_waitcnt vmcnt(39)
	v_mfma_f32_32x32x16_bf16 a[0:15], v[16:19], v[64:67], a[0:15]
	s_waitcnt vmcnt(38)
	v_mfma_f32_32x32x16_bf16 a[0:15], v[16:19], v[112:115], a[0:15]
	s_waitcnt vmcnt(37)
	v_mfma_f32_32x32x16_bf16 a[0:15], v[16:19], v[160:163], a[0:15]
	s_waitcnt vmcnt(36)
	v_mfma_f32_32x32x16_bf16 a[0:15], v[16:19], v[208:211], a[0:15]
	s_waitcnt vmcnt(35)
	v_mfma_f32_32x32x16_bf16 a[0:15], v[20:23], v[68:71], a[0:15]
	s_waitcnt vmcnt(34)
	v_mfma_f32_32x32x16_bf16 a[0:15], v[20:23], v[116:119], a[0:15]
	s_waitcnt vmcnt(33)
	v_mfma_f32_32x32x16_bf16 a[0:15], v[20:23], v[164:167], a[0:15]
	s_waitcnt vmcnt(32)
	v_mfma_f32_32x32x16_bf16 a[0:15], v[20:23], v[212:215], a[0:15]
	s_waitcnt vmcnt(31)
	v_mfma_f32_32x32x16_bf16 a[0:15], v[24:27], v[72:75], a[0:15]
	s_waitcnt vmcnt(30)
	v_mfma_f32_32x32x16_bf16 a[0:15], v[24:27], v[120:123], a[0:15]
	s_waitcnt vmcnt(29)
	v_mfma_f32_32x32x16_bf16 a[0:15], v[24:27], v[168:171], a[0:15]
	s_waitcnt vmcnt(28)
	v_mfma_f32_32x32x16_bf16 a[0:15], v[24:27], v[216:219], a[0:15]
	s_waitcnt vmcnt(27)
	v_mfma_f32_32x32x16_bf16 a[0:15], v[28:31], v[76:79], a[0:15]
	s_waitcnt vmcnt(26)
	v_mfma_f32_32x32x16_bf16 a[0:15], v[28:31], v[124:127], a[0:15]
	s_waitcnt vmcnt(25)
	v_mfma_f32_32x32x16_bf16 a[0:15], v[28:31], v[172:175], a[0:15]
	s_waitcnt vmcnt(24)
	v_mfma_f32_32x32x16_bf16 a[0:15], v[28:31], v[220:223], a[0:15]
	s_waitcnt vmcnt(23)
	v_mfma_f32_32x32x16_bf16 a[0:15], v[32:35], v[80:83], a[0:15]
	s_waitcnt vmcnt(22)
	v_mfma_f32_32x32x16_bf16 a[0:15], v[32:35], v[128:131], a[0:15]
	s_waitcnt vmcnt(21)
	v_mfma_f32_32x32x16_bf16 a[0:15], v[32:35], v[176:179], a[0:15]
	s_waitcnt vmcnt(20)
	v_mfma_f32_32x32x16_bf16 a[0:15], v[32:35], v[224:227], a[0:15]
	s_waitcnt vmcnt(19)
	v_mfma_f32_32x32x16_bf16 a[0:15], v[36:39], v[84:87], a[0:15]
	s_waitcnt vmcnt(18)
	v_mfma_f32_32x32x16_bf16 a[0:15], v[36:39], v[132:135], a[0:15]
	s_waitcnt vmcnt(17)
	v_mfma_f32_32x32x16_bf16 a[0:15], v[36:39], v[180:183], a[0:15]
	s_waitcnt vmcnt(16)
	v_mfma_f32_32x32x16_bf16 a[0:15], v[36:39], v[228:231], a[0:15]
	s_waitcnt vmcnt(15)
	v_mfma_f32_32x32x16_bf16 a[0:15], v[40:43], v[88:91], a[0:15]
	s_waitcnt vmcnt(14)
	v_mfma_f32_32x32x16_bf16 a[0:15], v[40:43], v[136:139], a[0:15]
	s_waitcnt vmcnt(13)
	v_mfma_f32_32x32x16_bf16 a[0:15], v[40:43], v[184:187], a[0:15]
	s_waitcnt vmcnt(12)
	v_mfma_f32_32x32x16_bf16 a[0:15], v[40:43], v[232:235], a[0:15]
	s_waitcnt vmcnt(11)
	v_mfma_f32_32x32x16_bf16 a[0:15], v[44:47], v[92:95], a[0:15]
	s_waitcnt vmcnt(10)
	v_mfma_f32_32x32x16_bf16 a[0:15], v[44:47], v[140:143], a[0:15]
	s_waitcnt vmcnt(9)
	v_mfma_f32_32x32x16_bf16 a[0:15], v[44:47], v[188:191], a[0:15]
	s_waitcnt vmcnt(8)
	v_mfma_f32_32x32x16_bf16 a[0:15], v[44:47], v[236:239], a[0:15]
	v_add_f32_e32 v8, 0, v248
	v_add_f32_e32 v8, v8, v249
	v_add_f32_e32 v8, v8, v250
	v_add_f32_e32 v8, v8, v251
	v_mov_b32_e32 v9, 0x3fb8aa3b
	s_waitcnt lgkmcnt(0)
	v_mul_f32_e32 v9, s22, v9
	v_exp_f32_e32 v9, v9
	v_add_f32_e32 v10, 0x2b8cbccc, v8
	v_div_scale_f32 v11, s[8:9], v10, v10, v9
	v_rcp_f32_e32 v12, v11
	v_div_scale_f32 v13, vcc, v9, v10, v9
	v_fma_f32 v14, -v11, v12, 1.0
	v_fmac_f32_e32 v12, v14, v12
	v_mul_f32_e32 v14, v13, v12
	v_fma_f32 v15, -v11, v14, v13
	v_fmac_f32_e32 v14, v15, v12
	v_fma_f32 v11, -v11, v14, v13
	v_div_fmas_f32 v11, v11, v12, v14
	v_div_fixup_f32 v9, v11, v10, v9
	v_lshlrev_b32_e32 v10, 2, v0
	v_add_u32_e32 v10, 0x4000, v10
	v_cmp_gt_u32_e32 vcc, 32, v0
	s_and_saveexec_b64 s[8:9], vcc
	ds_write2_b32 v10, v8, v9 offset0:128 offset1:160
	s_mov_b64 exec, s[8:9]
	s_waitcnt vmcnt(7)
	v_mfma_f32_32x32x16_bf16 a[0:15], v[48:51], v[96:99], a[0:15]
	s_waitcnt vmcnt(6)
	v_mfma_f32_32x32x16_bf16 a[0:15], v[48:51], v[144:147], a[0:15]
	s_waitcnt vmcnt(5)
	v_mfma_f32_32x32x16_bf16 a[0:15], v[48:51], v[192:195], a[0:15]
	s_waitcnt vmcnt(4)
	v_mfma_f32_32x32x16_bf16 a[0:15], v[48:51], v[240:243], a[0:15]
	v_mul_u32_u24_e32 v1, 0x1080, v1
	s_movk_i32 s4, 0x7f
	s_movk_i32 s6, 0x84
	v_cmp_lt_u32_e32 vcc, s4, v0
	v_lshrrev_b32_e32 v11, 3, v0
	v_and_b32_e32 v10, 31, v0
	v_and_b32_e32 v11, 4, v11
	v_mul_u32_u24_e32 v11, 0x84, v11
	v_lshlrev_b32_e32 v9, 2, v10
	v_bfe_u32 v6, v0, 2, 5
	v_and_b32_e32 v7, 3, v0
	v_add3_u32 v1, v1, v11, v9
	v_lshlrev_b32_e32 v8, 3, v7
	s_waitcnt vmcnt(3)
	v_mfma_f32_32x32x16_bf16 a[0:15], v[52:55], v[100:103], a[0:15]
	s_waitcnt vmcnt(2)
	v_mfma_f32_32x32x16_bf16 a[0:15], v[52:55], v[148:151], a[0:15]
	s_waitcnt vmcnt(1)
	v_mfma_f32_32x32x16_bf16 a[0:15], v[52:55], v[196:199], a[0:15]
	s_waitcnt vmcnt(0)
	v_mfma_f32_32x32x16_bf16 a[0:15], v[52:55], v[244:247], a[0:15]
	s_nop 11
	ds_write_b32 v1, a0
	ds_write_b32 v1, a1 offset:132
	ds_write_b32 v1, a2 offset:264
	ds_write_b32 v1, a3 offset:396
	ds_write_b32 v1, a4 offset:1056
	ds_write_b32 v1, a5 offset:1188
	ds_write_b32 v1, a6 offset:1320
	ds_write_b32 v1, a7 offset:1452
	ds_write_b32 v1, a8 offset:2112
	ds_write_b32 v1, a9 offset:2244
	ds_write_b32 v1, a10 offset:2376
	ds_write_b32 v1, a11 offset:2508
	ds_write_b32 v1, a12 offset:3168
	ds_write_b32 v1, a13 offset:3300
	ds_write_b32 v1, a14 offset:3432
	ds_write_b32 v1, a15 offset:3564
	v_bfe_u32 v6, v0, 2, 5
	v_and_b32_e32 v7, 3, v0
	v_lshlrev_b32_e32 v9, 3, v7
	v_readfirstlane_b32 s30, v0
	v_sub_u32_e32 v10, v6, v9
	s_waitcnt lgkmcnt(0)
	s_barrier
	s_cmpk_ge_u32 s30, 0x80
	s_cbranch_scc1 .Llg_k1
	v_mul_u32_u24_e32 v2, 0x84, v6
	v_lshlrev_b32_e32 v8, 5, v7
	v_add_u32_e32 v2, v2, v8
	v_add_u32_e32 v8, 0x4280, v8
	v_add_u32_e32 v3, 0x1080, v2
	v_add_u32_e32 v4, 0x2100, v2
	v_add_u32_e32 v5, 0x3180, v2
	ds_read_b128 v[48:51], v8
	ds_read_b128 v[52:55], v8 offset:16
	ds_read2_b32 v[16:17], v2 offset0:0 offset1:1
	ds_read2_b32 v[18:19], v2 offset0:2 offset1:3
	ds_read2_b32 v[20:21], v2 offset0:4 offset1:5
	ds_read2_b32 v[22:23], v2 offset0:6 offset1:7
	ds_read2_b32 v[24:25], v3 offset0:0 offset1:1
	ds_read2_b32 v[26:27], v3 offset0:2 offset1:3
	ds_read2_b32 v[28:29], v3 offset0:4 offset1:5
	ds_read2_b32 v[30:31], v3 offset0:6 offset1:7
	ds_read2_b32 v[32:33], v4 offset0:0 offset1:1
	ds_read2_b32 v[34:35], v4 offset0:2 offset1:3
	ds_read2_b32 v[36:37], v4 offset0:4 offset1:5
	ds_read2_b32 v[38:39], v4 offset0:6 offset1:7
	s_waitcnt lgkmcnt(4)
	ds_read2_b32 v[40:41], v5 offset0:0 offset1:1
	ds_read2_b32 v[42:43], v5 offset0:2 offset1:3
	ds_read2_b32 v[44:45], v5 offset0:4 offset1:5
	ds_read2_b32 v[46:47], v5 offset0:6 offset1:7
	s_waitcnt lgkmcnt(0)
	s_branch .Llg_join
